# stack26 = stack23 + expert-phase residual rows (x1) requested one dword per line at the start of the last down-projection k-step; relic waits in the tail block removed
# speedup vs baseline: 1.0051x; 1.0051x over previous
; #define MX(a_, b_, c_) __builtin_amdgcn_mfma_scale_f32_16x16x128_f8f6f4(a_, b_, c_, 0, 0, 0, 0x7f7f7f7f, 0, 0x7f7f7f7f)
; #define LD32(p_) CAT8(*(const i32x4v*)(p_), *(const i32x4v*)((p_) + 16))
; #define AFRAG(mi_, ks_) CAT8(*(const i32x4v*)(smem + aoff + (mi_) * 16384 + (((8 * (ks_) + 2 * g) ^ lr) << 4)), *(const i32x4v*)(smem + aoff + (mi_) * 16384 + (((8 * (ks_) + 2 * g + 1) ^ lr) << 4)))
; #define AFRAG(hb_, mi_, ks_) CAT8(*(const i32x4v*)((hb_) + aoff + (mi_) * 4096 + (((8 * (ks_) + 2 * g2) ^ lr2) << 4)), *(const i32x4v*)((hb_) + aoff + (mi_) * 4096 + (((8 * (ks_) + 2 * g2 + 1) ^ lr2) << 4)))
; #define LDX1(mi_, buf_) { const int tk_ = s_tok[16 * (mi_) + lr2]; const bf16_t* xr_ = X1B + (size_t)(tk_ < 0 ? 0 : tk_) * DM + 128 * wv + 4 * g2; \
;                 _Pragma("unroll") for (int c_ = 0; c_ < 8; ++c_) xb[buf_][c_] = *(const u32x2*)(xr_ + 16 * c_); }
; DEVINL void phase5(const Params& P, unsigned char* smem) {
;     ...
;                 for (int sk = 0; sk < 4; ++sk) {
;                     const int sn = 4 * ph + sk + 1 < 8 ? 4 * ph + sk + 1 : 7, sxn = (sn >> 1) & 1;
;                     const unsigned char* wn = wd0 + (size_t)(sxn ? e_hi : e_lo) * (2 * 64 * 2048) + (size_t)((sn & 1) * 64 + 4 * (sn >> 2)) * 2048;
;                     const unsigned char* hb = hs0 + (sk >> 1) * 20480;
;                     i32x8 fa[5];
; #pragma unroll
;                     for (int mi_ = 0; mi_ < 5; ++mi_) fa[mi_] = AFRAG(hb, mi_, sk & 1);
; #pragma unroll
;                     for (int j_ = 0; j_ < 4; ++j_) {
; #pragma unroll
;                         for (int mi_ = 0; mi_ < 5; ++mi_) acc[j_][mi_] = MX(b0[j_], fa[mi_], acc[j_][mi_]);
;                         b0[j_] = LD32(wn + j_ * 2048 + voff2);
;                         __builtin_amdgcn_sched_barrier(0);
;                     }
;     ...
;             LDX1(0, 0)
.LBB0_727:
	s_min_u32 s29, s28, 2
	s_add_i32 s29, s29, 5
	s_bitcmp0_b32 s29, 1
	s_cselect_b32 s30, s49, s0
	s_lshr_b32 s31, s28, 1
	s_mulk_i32 s31, 0x5000
	s_and_b32 s34, s1, 8
	v_add_u32_e32 v199, s31, v196
	s_lshl_b32 s29, s29, 17
	s_ashr_i32 s31, s30, 31
	v_add_u32_e32 v198, s34, v197
	s_and_b32 s29, s29, 0x20000
	s_lshl_b64 s[30:31], s[30:31], 18
	v_xor_b32_e32 v200, v198, v225
	v_bitop3_b32 v198, v198, v225, 1 bitop3:0x36
	s_add_u32 s30, s39, s30
	v_lshl_add_u32 v214, v200, 4, v199
	v_lshl_add_u32 v215, v198, 4, v199
	s_addc_u32 s31, s40, s31
	ds_read_b128 v[202:205], v215
	ds_read_b128 v[198:201], v214
	ds_read_b128 v[206:209], v214 offset:4096
	ds_read_b128 v[226:229], v214 offset:16384
	ds_read_b128 v[210:213], v215 offset:4096
	ds_read_b128 v[238:241], v215 offset:8192
	ds_read_b128 v[234:237], v214 offset:8192
	ds_read_b128 v[242:245], v214 offset:12288
	ds_read_b128 v[246:249], v215 offset:12288
	ds_read_b128 v[230:233], v215 offset:16384
	s_add_u32 s30, s30, s29
	s_addc_u32 s31, s31, 0
	v_lshl_add_u64 v[214:215], s[30:31], 0, v[194:195]
	v_add_co_u32_e32 v218, vcc, s47, v214
	s_waitcnt vmcnt(6) lgkmcnt(8)
	v_mfma_scale_f32_16x16x128_f8f6f4 v[190:193], v[2:9], v[198:205], v[190:193], v220, v220 op_sel_hi:[0,0,0]
	v_addc_co_u32_e32 v219, vcc, 0, v215, vcc
	v_lshl_add_u64 v[216:217], v[214:215], 0, s[20:21]
	s_waitcnt lgkmcnt(5)
	v_mfma_scale_f32_16x16x128_f8f6f4 v[186:189], v[2:9], v[206:213], v[186:189], v220, v220 op_sel_hi:[0,0,0]
	s_waitcnt lgkmcnt(3)
	v_mfma_scale_f32_16x16x128_f8f6f4 v[182:185], v[2:9], v[234:241], v[182:185], v220, v220 op_sel_hi:[0,0,0]
	s_waitcnt lgkmcnt(1)
	v_mfma_scale_f32_16x16x128_f8f6f4 v[178:181], v[2:9], v[242:249], v[178:181], v220, v220 op_sel_hi:[0,0,0]
	s_waitcnt lgkmcnt(0)
	v_mfma_scale_f32_16x16x128_f8f6f4 v[174:177], v[2:9], v[226:233], v[174:177], v220, v220 op_sel_hi:[0,0,0]
	global_load_dwordx4 v[2:5], v[218:219], off offset:-4096
	global_load_dwordx4 v[6:9], v[216:217], off offset:16
	s_waitcnt vmcnt(6)
	v_mfma_scale_f32_16x16x128_f8f6f4 v[170:173], v[10:17], v[198:205], v[170:173], v220, v220 op_sel_hi:[0,0,0]
	v_mfma_scale_f32_16x16x128_f8f6f4 v[166:169], v[10:17], v[206:213], v[166:169], v220, v220 op_sel_hi:[0,0,0]
	v_mfma_scale_f32_16x16x128_f8f6f4 v[162:165], v[10:17], v[234:241], v[162:165], v220, v220 op_sel_hi:[0,0,0]
	v_mfma_scale_f32_16x16x128_f8f6f4 v[158:161], v[10:17], v[242:249], v[158:161], v220, v220 op_sel_hi:[0,0,0]
	v_mfma_scale_f32_16x16x128_f8f6f4 v[154:157], v[10:17], v[226:233], v[154:157], v220, v220 op_sel_hi:[0,0,0]
	global_load_dwordx4 v[10:13], v[216:217], off offset:2048
	global_load_dwordx4 v[14:17], v[216:217], off offset:2064
	s_waitcnt vmcnt(6)
	v_mfma_scale_f32_16x16x128_f8f6f4 v[150:153], v[18:25], v[198:205], v[150:153], v220, v220 op_sel_hi:[0,0,0]
	v_lshl_add_u64 v[216:217], v[214:215], 0, s[22:23]
	v_mfma_scale_f32_16x16x128_f8f6f4 v[146:149], v[18:25], v[206:213], v[146:149], v220, v220 op_sel_hi:[0,0,0]
	v_mfma_scale_f32_16x16x128_f8f6f4 v[142:145], v[18:25], v[234:241], v[142:145], v220, v220 op_sel_hi:[0,0,0]
	v_mfma_scale_f32_16x16x128_f8f6f4 v[138:141], v[18:25], v[242:249], v[138:141], v220, v220 op_sel_hi:[0,0,0]
	v_mfma_scale_f32_16x16x128_f8f6f4 v[134:137], v[18:25], v[226:233], v[134:137], v220, v220 op_sel_hi:[0,0,0]
	global_load_dwordx4 v[18:21], v[218:219], off
	global_load_dwordx4 v[22:25], v[216:217], off offset:16
	s_waitcnt vmcnt(6)
	v_mfma_scale_f32_16x16x128_f8f6f4 v[130:133], v[26:33], v[198:205], v[130:133], v220, v220 op_sel_hi:[0,0,0]
	v_lshl_add_u64 v[198:199], v[214:215], 0, s[24:25]
	v_mfma_scale_f32_16x16x128_f8f6f4 v[126:129], v[26:33], v[206:213], v[126:129], v220, v220 op_sel_hi:[0,0,0]
	v_mfma_scale_f32_16x16x128_f8f6f4 v[122:125], v[26:33], v[234:241], v[122:125], v220, v220 op_sel_hi:[0,0,0]
	v_mfma_scale_f32_16x16x128_f8f6f4 v[118:121], v[26:33], v[242:249], v[118:121], v220, v220 op_sel_hi:[0,0,0]
	v_mfma_scale_f32_16x16x128_f8f6f4 v[114:117], v[26:33], v[226:233], v[114:117], v220, v220 op_sel_hi:[0,0,0]
	global_load_dwordx4 v[26:29], v[218:219], off offset:2048
	global_load_dwordx4 v[30:33], v[198:199], off offset:16
	s_add_i32 s28, s28, 1
	s_add_i32 s1, s1, 8
	s_cmp_lg_u32 s28, 3
	s_cbranch_scc1 .LBB0_727
	v_lshrrev_b32_e32 v250, 1, v224
	v_lshl_add_u32 v250, v250, 4, v225
	v_lshlrev_b32_e32 v250, 2, v250
	v_add_u32_e32 v250, 0x24900, v250
	v_lshlrev_b32_e32 v253, 2, v225
	v_add_u32_e32 v253, 0x24a00, v253
	ds_read_b32 v251, v250
	ds_read_b32 v252, v250 offset:128
	ds_read_b32 v253, v253
	v_and_b32_e32 v250, 1, v224
	v_lshlrev_b32_e32 v250, 7, v250
	s_waitcnt lgkmcnt(0)
	v_max_i32_e32 v251, 0, v251
	v_max_i32_e32 v252, 0, v252
	v_max_i32_e32 v253, 0, v253
	v_lshl_add_u32 v251, v251, 11, v250
	v_lshl_add_u32 v252, v252, 11, v250
	v_lshl_add_u32 v253, v253, 11, v250
	global_load_dword v251, v251, s[10:11]
	global_load_dword v252, v252, s[10:11]
	global_load_dword v253, v253, s[10:11]
	s_min_u32 s29, s28, 2
	s_add_i32 s29, s29, 5
	s_bitcmp0_b32 s29, 1
	s_cselect_b32 s30, s49, s0
	s_lshr_b32 s31, s28, 1
	s_mulk_i32 s31, 0x5000
	s_and_b32 s34, s1, 8
	v_add_u32_e32 v199, s31, v196
	s_lshl_b32 s29, s29, 17
	s_ashr_i32 s31, s30, 31
	v_add_u32_e32 v198, s34, v197
	s_and_b32 s29, s29, 0x20000
	s_lshl_b64 s[30:31], s[30:31], 18
	v_xor_b32_e32 v200, v198, v225
	v_bitop3_b32 v198, v198, v225, 1 bitop3:0x36
	s_add_u32 s30, s39, s30
	v_lshl_add_u32 v214, v200, 4, v199
	v_lshl_add_u32 v215, v198, 4, v199
	s_addc_u32 s31, s40, s31
	ds_read_b128 v[202:205], v215
	ds_read_b128 v[198:201], v214
	ds_read_b128 v[206:209], v214 offset:4096
	ds_read_b128 v[226:229], v214 offset:16384
	ds_read_b128 v[210:213], v215 offset:4096
	ds_read_b128 v[238:241], v215 offset:8192
	ds_read_b128 v[234:237], v214 offset:8192
	ds_read_b128 v[242:245], v214 offset:12288
	ds_read_b128 v[246:249], v215 offset:12288
	ds_read_b128 v[230:233], v215 offset:16384
	s_add_u32 s30, s30, s29
	s_addc_u32 s31, s31, 0
	v_lshl_add_u64 v[214:215], s[30:31], 0, v[194:195]
	v_add_co_u32_e32 v218, vcc, s47, v214
	s_waitcnt vmcnt(9) lgkmcnt(8)
; DEVINL unsigned pk2(float lo, float hi) { const f32x2 v = {lo, hi}; return __builtin_bit_cast(unsigned, __builtin_convertvector(v, bf16v2)); }
; #define MX(a_, b_, c_) __builtin_amdgcn_mfma_scale_f32_16x16x128_f8f6f4(a_, b_, c_, 0, 0, 0, 0x7f7f7f7f, 0, 0x7f7f7f7f)
; #define LD32(p_) CAT8(*(const i32x4v*)(p_), *(const i32x4v*)((p_) + 16))
; #define AFRAG(mi_, ks_) CAT8(*(const i32x4v*)(smem + aoff + (mi_) * 16384 + (((8 * (ks_) + 2 * g) ^ lr) << 4)), *(const i32x4v*)(smem + aoff + (mi_) * 16384 + (((8 * (ks_) + 2 * g + 1) ^ lr) << 4)))
; #define AFRAG(hb_, mi_, ks_) CAT8(*(const i32x4v*)((hb_) + aoff + (mi_) * 4096 + (((8 * (ks_) + 2 * g2) ^ lr2) << 4)), *(const i32x4v*)((hb_) + aoff + (mi_) * 4096 + (((8 * (ks_) + 2 * g2 + 1) ^ lr2) << 4)))
; DEVINL void phase5(const Params& P, unsigned char* smem) {
;     ...
;                     for (int mi_ = 0; mi_ < 5; ++mi_) fa[mi_] = AFRAG(hb, mi_, sk & 1);
; #pragma unroll
;                     for (int j_ = 0; j_ < 4; ++j_) {
; #pragma unroll
;                         for (int mi_ = 0; mi_ < 5; ++mi_) acc[j_][mi_] = MX(b0[j_], fa[mi_], acc[j_][mi_]);
;                         b0[j_] = LD32(wn + j_ * 2048 + voff2);
;                         __builtin_amdgcn_sched_barrier(0);
;                     }
;                 }
; #pragma unroll
;                 for (int i = 0; i < 4; ++i)
; #pragma unroll
;                     for (int mi = 0; mi < 5; ++mi) {
;                         const f32x4 v = acc[i][mi] * (1.f / 128.f);
;                         q[mi] += v.x * v.x + v.y * v.y + v.z * v.z + v.w * v.w;
;                         if (ph == 0) { ypk[i][mi].x = pk2(v.x, v.y); ypk[i][mi].y = pk2(v.z, v.w); } else acc[i][mi] = v;
	v_mfma_scale_f32_16x16x128_f8f6f4 v[190:193], v[2:9], v[198:205], v[190:193], v220, v220 op_sel_hi:[0,0,0]
	v_addc_co_u32_e32 v219, vcc, 0, v215, vcc
	v_lshl_add_u64 v[216:217], v[214:215], 0, s[20:21]
	s_waitcnt lgkmcnt(5)
	v_mfma_scale_f32_16x16x128_f8f6f4 v[186:189], v[2:9], v[206:213], v[186:189], v220, v220 op_sel_hi:[0,0,0]
	s_waitcnt lgkmcnt(3)
	v_mfma_scale_f32_16x16x128_f8f6f4 v[182:185], v[2:9], v[234:241], v[182:185], v220, v220 op_sel_hi:[0,0,0]
	s_waitcnt lgkmcnt(1)
	v_mfma_scale_f32_16x16x128_f8f6f4 v[178:181], v[2:9], v[242:249], v[178:181], v220, v220 op_sel_hi:[0,0,0]
	s_waitcnt lgkmcnt(0)
	v_mfma_scale_f32_16x16x128_f8f6f4 v[174:177], v[2:9], v[226:233], v[174:177], v220, v220 op_sel_hi:[0,0,0]
	s_waitcnt vmcnt(7)
	v_mfma_scale_f32_16x16x128_f8f6f4 v[170:173], v[10:17], v[198:205], v[170:173], v220, v220 op_sel_hi:[0,0,0]
	v_mfma_scale_f32_16x16x128_f8f6f4 v[166:169], v[10:17], v[206:213], v[166:169], v220, v220 op_sel_hi:[0,0,0]
	v_mfma_scale_f32_16x16x128_f8f6f4 v[162:165], v[10:17], v[234:241], v[162:165], v220, v220 op_sel_hi:[0,0,0]
	v_mfma_scale_f32_16x16x128_f8f6f4 v[158:161], v[10:17], v[242:249], v[158:161], v220, v220 op_sel_hi:[0,0,0]
	v_mfma_scale_f32_16x16x128_f8f6f4 v[154:157], v[10:17], v[226:233], v[154:157], v220, v220 op_sel_hi:[0,0,0]
	s_waitcnt vmcnt(5)
	v_mfma_scale_f32_16x16x128_f8f6f4 v[150:153], v[18:25], v[198:205], v[150:153], v220, v220 op_sel_hi:[0,0,0]
	v_lshl_add_u64 v[216:217], v[214:215], 0, s[22:23]
	v_mfma_scale_f32_16x16x128_f8f6f4 v[146:149], v[18:25], v[206:213], v[146:149], v220, v220 op_sel_hi:[0,0,0]
	v_mfma_scale_f32_16x16x128_f8f6f4 v[142:145], v[18:25], v[234:241], v[142:145], v220, v220 op_sel_hi:[0,0,0]
	v_mfma_scale_f32_16x16x128_f8f6f4 v[138:141], v[18:25], v[242:249], v[138:141], v220, v220 op_sel_hi:[0,0,0]
	v_mfma_scale_f32_16x16x128_f8f6f4 v[134:137], v[18:25], v[226:233], v[134:137], v220, v220 op_sel_hi:[0,0,0]
	s_waitcnt vmcnt(3)
	v_mfma_scale_f32_16x16x128_f8f6f4 v[130:133], v[26:33], v[198:205], v[130:133], v220, v220 op_sel_hi:[0,0,0]
	v_lshl_add_u64 v[198:199], v[214:215], 0, s[24:25]
	v_mfma_scale_f32_16x16x128_f8f6f4 v[126:129], v[26:33], v[206:213], v[126:129], v220, v220 op_sel_hi:[0,0,0]
	v_mfma_scale_f32_16x16x128_f8f6f4 v[122:125], v[26:33], v[234:241], v[122:125], v220, v220 op_sel_hi:[0,0,0]
	v_mfma_scale_f32_16x16x128_f8f6f4 v[118:121], v[26:33], v[242:249], v[118:121], v220, v220 op_sel_hi:[0,0,0]
	v_mfma_scale_f32_16x16x128_f8f6f4 v[114:117], v[26:33], v[226:233], v[114:117], v220, v220 op_sel_hi:[0,0,0]
	v_pk_mul_f32 v[206:207], v[110:111], s[26:27] op_sel_hi:[1,0]
	v_pk_mul_f32 v[210:211], v[90:91], s[26:27] op_sel_hi:[1,0]
	v_mul_f32_e32 v10, v207, v207
	v_mul_f32_e32 v17, v211, v211
	v_pk_mul_f32 v[204:205], v[112:113], s[26:27] op_sel_hi:[1,0]
	v_pk_mul_f32 v[208:209], v[92:93], s[26:27] op_sel_hi:[1,0]
	v_fmac_f32_e32 v17, v210, v210
	v_pk_mul_f32 v[214:215], v[70:71], s[26:27] op_sel_hi:[1,0]
	v_fmac_f32_e32 v10, v206, v206
	v_fmac_f32_e32 v17, v208, v208
	v_mul_f32_e32 v28, v215, v215
	v_pk_mul_f32 v[218:219], v[50:51], s[26:27] op_sel_hi:[1,0]
	v_fmac_f32_e32 v10, v204, v204
	v_fmac_f32_e32 v17, v209, v209
	v_pk_mul_f32 v[212:213], v[72:73], s[26:27] op_sel_hi:[1,0]
	v_fmac_f32_e32 v28, v214, v214
	v_mul_f32_e32 v33, v219, v219
	v_fmac_f32_e32 v10, v205, v205
	v_pk_mul_f32 v[190:191], v[190:191], s[26:27] op_sel_hi:[1,0]
	v_pk_mul_f32 v[106:107], v[106:107], s[26:27] op_sel_hi:[1,0]
	v_pk_mul_f32 v[2:3], v[96:97], s[26:27] op_sel_hi:[1,0]
	v_pk_mul_f32 v[96:97], v[86:87], s[26:27] op_sel_hi:[1,0]
	v_fmac_f32_e32 v28, v212, v212
	v_pk_mul_f32 v[216:217], v[52:53], s[26:27] op_sel_hi:[1,0]
	v_fmac_f32_e32 v33, v218, v218
	v_add_f32_e32 v10, v10, v17
	v_mul_f32_e32 v17, v191, v191
	v_mul_f32_e32 v11, v107, v107
	v_mul_f32_e32 v18, v97, v97
	v_fmac_f32_e32 v28, v213, v213
	v_pk_mul_f32 v[198:199], v[66:67], s[26:27] op_sel_hi:[1,0]
	v_fmac_f32_e32 v33, v216, v216
	v_pk_mul_f32 v[192:193], v[192:193], s[26:27] op_sel_hi:[1,0]
	v_fmac_f32_e32 v17, v190, v190
	v_pk_mul_f32 v[108:109], v[108:109], s[26:27] op_sel_hi:[1,0]
	v_pk_mul_f32 v[4:5], v[94:95], s[26:27] op_sel_hi:[1,0]
	v_pk_mul_f32 v[94:95], v[88:89], s[26:27] op_sel_hi:[1,0]
	v_fmac_f32_e32 v18, v96, v96
	v_mul_f32_e32 v29, v199, v199
	v_fmac_f32_e32 v33, v217, v217
	v_pk_mul_f32 v[202:203], v[46:47], s[26:27] op_sel_hi:[1,0]
	v_fmac_f32_e32 v11, v106, v106
	v_add_f32_e32 v10, v10, v28
	v_fmac_f32_e32 v17, v192, v192
	v_fmac_f32_e32 v18, v94, v94
	v_pk_mul_f32 v[196:197], v[68:69], s[26:27] op_sel_hi:[1,0]
	v_fmac_f32_e32 v29, v198, v198
	v_mul_f32_e32 v46, v203, v203
	v_fmac_f32_e32 v11, v108, v108
	v_add_f32_e32 v10, v10, v33
	v_fmac_f32_e32 v17, v193, v193
	v_pk_mul_f32 v[112:113], v[186:187], s[26:27] op_sel_hi:[1,0]
	v_pk_mul_f32 v[102:103], v[102:103], s[26:27] op_sel_hi:[1,0]
	v_fmac_f32_e32 v18, v95, v95
	v_pk_mul_f32 v[82:83], v[82:83], s[26:27] op_sel_hi:[1,0]
	v_fmac_f32_e32 v29, v196, v196
	v_pk_mul_f32 v[200:201], v[48:49], s[26:27] op_sel_hi:[1,0]
	v_fmac_f32_e32 v46, v202, v202
	v_fmac_f32_e32 v11, v109, v109
	v_add_f32_e32 v17, v10, v17
	v_mul_f32_e32 v10, v113, v113
	v_mul_f32_e32 v12, v103, v103
	v_mul_f32_e32 v19, v83, v83
	v_fmac_f32_e32 v29, v197, v197
	v_pk_mul_f32 v[70:71], v[62:63], s[26:27] op_sel_hi:[1,0]
	v_fmac_f32_e32 v46, v200, v200
	v_add_f32_e32 v11, v11, v18
	v_pk_mul_f32 v[110:111], v[188:189], s[26:27] op_sel_hi:[1,0]
	v_fmac_f32_e32 v10, v112, v112
	v_pk_mul_f32 v[104:105], v[104:105], s[26:27] op_sel_hi:[1,0]
	v_pk_mul_f32 v[84:85], v[84:85], s[26:27] op_sel_hi:[1,0]
	v_fmac_f32_e32 v19, v82, v82
	v_pk_mul_f32 v[8:9], v[74:75], s[26:27] op_sel_hi:[1,0]
; DEVINL unsigned pk2(float lo, float hi) { const f32x2 v = {lo, hi}; return __builtin_bit_cast(unsigned, __builtin_convertvector(v, bf16v2)); }
; DEVINL void phase5(const Params& P, unsigned char* smem) {
;     ...
; #pragma unroll
;                 for (int i = 0; i < 4; ++i)
; #pragma unroll
;                     for (int mi = 0; mi < 5; ++mi) {
;                         const f32x4 v = acc[i][mi] * (1.f / 128.f);
;                         q[mi] += v.x * v.x + v.y * v.y + v.z * v.z + v.w * v.w;
;                         if (ph == 0) { ypk[i][mi].x = pk2(v.x, v.y); ypk[i][mi].y = pk2(v.z, v.w); } else acc[i][mi] = v;
;                     }
	v_mul_f32_e32 v30, v71, v71
	v_fmac_f32_e32 v46, v201, v201
	v_pk_mul_f32 v[74:75], v[42:43], s[26:27] op_sel_hi:[1,0]
	v_fmac_f32_e32 v12, v102, v102
	v_add_f32_e32 v11, v11, v29
	v_fmac_f32_e32 v10, v110, v110
	v_mul_f32_e32 v16, v5, v5
	v_fmac_f32_e32 v19, v84, v84
	v_mul_f32_e32 v27, v9, v9
	v_pk_mul_f32 v[64:65], v[64:65], s[26:27] op_sel_hi:[1,0]
	v_fmac_f32_e32 v30, v70, v70
	v_pk_mul_f32 v[20:21], v[54:55], s[26:27] op_sel_hi:[1,0]
	v_mul_f32_e32 v47, v75, v75
	v_fmac_f32_e32 v12, v104, v104
	v_add_f32_e32 v11, v11, v46
	v_fmac_f32_e32 v10, v111, v111
	v_pk_mul_f32 v[62:63], v[182:183], s[26:27] op_sel_hi:[1,0]
	v_pk_mul_f32 v[98:99], v[98:99], s[26:27] op_sel_hi:[1,0]
	v_fmac_f32_e32 v19, v85, v85
	v_pk_mul_f32 v[78:79], v[78:79], s[26:27] op_sel_hi:[1,0]
	v_pk_mul_f32 v[6:7], v[76:77], s[26:27] op_sel_hi:[1,0]
	v_fmac_f32_e32 v27, v8, v8
	v_fmac_f32_e32 v30, v64, v64
	v_mul_f32_e32 v32, v21, v21
	v_pk_mul_f32 v[72:73], v[44:45], s[26:27] op_sel_hi:[1,0]
	v_fmac_f32_e32 v47, v74, v74
	v_pk_mul_f32 v[24:25], v[34:35], s[26:27] op_sel_hi:[1,0]
	v_fmac_f32_e32 v12, v105, v105
	v_fmac_f32_e32 v16, v4, v4
	v_add_f32_e32 v18, v11, v10
	v_mul_f32_e32 v10, v63, v63
	v_mul_f32_e32 v13, v99, v99
	v_mul_f32_e32 v26, v79, v79
	v_fmac_f32_e32 v27, v6, v6
	v_fmac_f32_e32 v30, v65, v65
	v_pk_mul_f32 v[58:59], v[58:59], s[26:27] op_sel_hi:[1,0]
	v_pk_mul_f32 v[14:15], v[56:57], s[26:27] op_sel_hi:[1,0]
	v_fmac_f32_e32 v32, v20, v20
	v_fmac_f32_e32 v47, v72, v72
	v_mul_f32_e32 v34, v25, v25
	v_fmac_f32_e32 v16, v2, v2
	v_add_f32_e32 v12, v12, v19
	v_pk_mul_f32 v[56:57], v[184:185], s[26:27] op_sel_hi:[1,0]
	v_fmac_f32_e32 v10, v62, v62
	v_pk_mul_f32 v[100:101], v[100:101], s[26:27] op_sel_hi:[1,0]
	v_pk_mul_f32 v[80:81], v[80:81], s[26:27] op_sel_hi:[1,0]
	v_fmac_f32_e32 v26, v78, v78
	v_fmac_f32_e32 v27, v7, v7
	v_mul_f32_e32 v31, v59, v59
	v_fmac_f32_e32 v32, v14, v14
	v_fmac_f32_e32 v47, v73, v73
	v_pk_mul_f32 v[44:45], v[38:39], s[26:27] op_sel_hi:[1,0]
	v_pk_mul_f32 v[22:23], v[36:37], s[26:27] op_sel_hi:[1,0]
	v_fmac_f32_e32 v34, v24, v24
	v_fmac_f32_e32 v13, v98, v98
	v_fmac_f32_e32 v16, v3, v3
	v_add_f32_e32 v12, v12, v30
	v_fmac_f32_e32 v10, v56, v56
	v_fmac_f32_e32 v26, v80, v80
	v_pk_mul_f32 v[60:61], v[60:61], s[26:27] op_sel_hi:[1,0]
	v_fmac_f32_e32 v31, v58, v58
	v_fmac_f32_e32 v32, v15, v15
	v_mul_f32_e32 v38, v45, v45
	v_fmac_f32_e32 v34, v22, v22
	v_fmac_f32_e32 v13, v100, v100
	v_add_f32_e32 v16, v16, v27
	v_add_f32_e32 v12, v12, v47
	v_fmac_f32_e32 v10, v57, v57
	v_pk_mul_f32 v[36:37], v[178:179], s[26:27] op_sel_hi:[1,0]
	v_fmac_f32_e32 v26, v81, v81
	v_fmac_f32_e32 v31, v60, v60
	v_pk_mul_f32 v[42:43], v[40:41], s[26:27] op_sel_hi:[1,0]
	v_fmac_f32_e32 v38, v44, v44
	v_fmac_f32_e32 v34, v23, v23
	v_fmac_f32_e32 v13, v101, v101
	v_add_f32_e32 v16, v16, v32
	v_add_f32_e32 v19, v12, v10
	v_mul_f32_e32 v10, v37, v37
	v_fmac_f32_e32 v31, v61, v61
	v_fmac_f32_e32 v38, v42, v42
	v_add_f32_e32 v13, v13, v26
	v_add_f32_e32 v16, v16, v34
	v_pk_mul_f32 v[34:35], v[180:181], s[26:27] op_sel_hi:[1,0]
	v_fmac_f32_e32 v10, v36, v36
	v_fmac_f32_e32 v38, v43, v43
	v_add_f32_e32 v13, v13, v31
	v_fmac_f32_e32 v10, v34, v34
	v_add_f32_e32 v13, v13, v38
	v_fmac_f32_e32 v10, v35, v35
	v_add_f32_e32 v26, v13, v10
	v_pk_mul_f32 v[12:13], v[174:175], s[26:27] op_sel_hi:[1,0]
	v_pk_mul_f32 v[10:11], v[176:177], s[26:27] op_sel_hi:[1,0]
	v_mul_f32_e32 v27, v13, v13
	v_fmac_f32_e32 v27, v12, v12
	v_fmac_f32_e32 v27, v10, v10
	v_fmac_f32_e32 v27, v11, v11
	v_pk_mul_f32 v[170:171], v[170:171], s[26:27] op_sel_hi:[1,0]
	v_add_f32_e32 v27, v16, v27
	v_mul_f32_e32 v16, v171, v171
	v_pk_mul_f32 v[172:173], v[172:173], s[26:27] op_sel_hi:[1,0]
	v_fmac_f32_e32 v16, v170, v170
	v_fmac_f32_e32 v16, v172, v172
	v_fmac_f32_e32 v16, v173, v173
	v_pk_mul_f32 v[166:167], v[166:167], s[26:27] op_sel_hi:[1,0]
	v_add_f32_e32 v28, v17, v16
	v_mul_f32_e32 v16, v167, v167
	v_pk_mul_f32 v[168:169], v[168:169], s[26:27] op_sel_hi:[1,0]
	v_fmac_f32_e32 v16, v166, v166
	v_fmac_f32_e32 v16, v168, v168
	v_fmac_f32_e32 v16, v169, v169
	v_pk_mul_f32 v[68:69], v[162:163], s[26:27] op_sel_hi:[1,0]
	v_add_f32_e32 v29, v18, v16
	v_mul_f32_e32 v16, v69, v69
	v_pk_mul_f32 v[66:67], v[164:165], s[26:27] op_sel_hi:[1,0]
	v_fmac_f32_e32 v16, v68, v68
	v_fmac_f32_e32 v16, v66, v66
	v_fmac_f32_e32 v16, v67, v67
	v_pk_mul_f32 v[40:41], v[158:159], s[26:27] op_sel_hi:[1,0]
	v_add_f32_e32 v30, v19, v16
; DEVINL unsigned pk2(float lo, float hi) { const f32x2 v = {lo, hi}; return __builtin_bit_cast(unsigned, __builtin_convertvector(v, bf16v2)); }
; DEVINL void phase5(const Params& P, unsigned char* smem) {
;     ...
; #pragma unroll
;                 for (int i = 0; i < 4; ++i)
; #pragma unroll
;                     for (int mi = 0; mi < 5; ++mi) {
;                         const f32x4 v = acc[i][mi] * (1.f / 128.f);
;                         q[mi] += v.x * v.x + v.y * v.y + v.z * v.z + v.w * v.w;
;                         if (ph == 0) { ypk[i][mi].x = pk2(v.x, v.y); ypk[i][mi].y = pk2(v.z, v.w); } else acc[i][mi] = v;
;                     }
;             }
;     ...
; #pragma unroll
;             for (int mi = 0; mi < 5; ++mi) { q[mi] = gsum4(q[mi]); }
;             if (g2 == 0) {
; #pragma unroll
;                 for (int mi = 0; mi < 5; ++mi) s_part[wv * 80 + 16 * mi + lr2] = q[mi];
;             }
	v_mul_f32_e32 v16, v41, v41
	v_pk_mul_f32 v[38:39], v[160:161], s[26:27] op_sel_hi:[1,0]
	v_fmac_f32_e32 v16, v40, v40
	v_fmac_f32_e32 v16, v38, v38
	v_pk_mul_f32 v[18:19], v[154:155], s[26:27] op_sel_hi:[1,0]
	v_fmac_f32_e32 v16, v39, v39
	v_mul_f32_e32 v31, v19, v19
	v_add_f32_e32 v26, v26, v16
	v_pk_mul_f32 v[16:17], v[156:157], s[26:27] op_sel_hi:[1,0]
	v_fmac_f32_e32 v31, v18, v18
	v_fmac_f32_e32 v31, v16, v16
	v_fmac_f32_e32 v31, v17, v17
	v_pk_mul_f32 v[150:151], v[150:151], s[26:27] op_sel_hi:[1,0]
	v_add_f32_e32 v31, v27, v31
	v_mul_f32_e32 v27, v151, v151
	v_pk_mul_f32 v[152:153], v[152:153], s[26:27] op_sel_hi:[1,0]
	v_fmac_f32_e32 v27, v150, v150
	v_fmac_f32_e32 v27, v152, v152
	v_fmac_f32_e32 v27, v153, v153
	v_pk_mul_f32 v[146:147], v[146:147], s[26:27] op_sel_hi:[1,0]
	v_add_f32_e32 v32, v28, v27
	v_mul_f32_e32 v27, v147, v147
	v_pk_mul_f32 v[148:149], v[148:149], s[26:27] op_sel_hi:[1,0]
	v_fmac_f32_e32 v27, v146, v146
	v_fmac_f32_e32 v27, v148, v148
	v_fmac_f32_e32 v27, v149, v149
	v_pk_mul_f32 v[86:87], v[142:143], s[26:27] op_sel_hi:[1,0]
	v_add_f32_e32 v33, v29, v27
	v_mul_f32_e32 v27, v87, v87
	v_pk_mul_f32 v[76:77], v[144:145], s[26:27] op_sel_hi:[1,0]
	v_fmac_f32_e32 v27, v86, v86
	v_fmac_f32_e32 v27, v76, v76
	v_fmac_f32_e32 v27, v77, v77
	v_pk_mul_f32 v[48:49], v[138:139], s[26:27] op_sel_hi:[1,0]
	v_add_f32_e32 v30, v30, v27
	v_mul_f32_e32 v27, v49, v49
	v_pk_mul_f32 v[46:47], v[140:141], s[26:27] op_sel_hi:[1,0]
	v_fmac_f32_e32 v27, v48, v48
	v_fmac_f32_e32 v27, v46, v46
	v_pk_mul_f32 v[28:29], v[134:135], s[26:27] op_sel_hi:[1,0]
	v_fmac_f32_e32 v27, v47, v47
	v_mul_f32_e32 v50, v29, v29
	v_add_f32_e32 v54, v26, v27
	v_pk_mul_f32 v[26:27], v[136:137], s[26:27] op_sel_hi:[1,0]
	v_fmac_f32_e32 v50, v28, v28
	v_fmac_f32_e32 v50, v26, v26
	v_fmac_f32_e32 v50, v27, v27
	v_pk_mul_f32 v[136:137], v[130:131], s[26:27] op_sel_hi:[1,0]
	v_add_f32_e32 v55, v31, v50
	v_mul_f32_e32 v31, v137, v137
	v_pk_mul_f32 v[132:133], v[132:133], s[26:27] op_sel_hi:[1,0]
	v_fmac_f32_e32 v31, v136, v136
	v_fmac_f32_e32 v31, v132, v132
	v_fmac_f32_e32 v31, v133, v133
	v_pk_mul_f32 v[126:127], v[126:127], s[26:27] op_sel_hi:[1,0]
	v_add_f32_e32 v92, v32, v31
	v_mul_f32_e32 v31, v127, v127
	v_pk_mul_f32 v[128:129], v[128:129], s[26:27] op_sel_hi:[1,0]
	v_fmac_f32_e32 v31, v126, v126
	v_fmac_f32_e32 v31, v128, v128
	v_fmac_f32_e32 v31, v129, v129
	v_pk_mul_f32 v[90:91], v[122:123], s[26:27] op_sel_hi:[1,0]
	v_add_f32_e32 v93, v33, v31
	v_mul_f32_e32 v31, v91, v91
	v_pk_mul_f32 v[88:89], v[124:125], s[26:27] op_sel_hi:[1,0]
	v_fmac_f32_e32 v31, v90, v90
	v_fmac_f32_e32 v31, v88, v88
	v_fmac_f32_e32 v31, v89, v89
	v_pk_mul_f32 v[52:53], v[118:119], s[26:27] op_sel_hi:[1,0]
	v_add_f32_e32 v122, v30, v31
	v_mul_f32_e32 v30, v53, v53
	v_pk_mul_f32 v[50:51], v[120:121], s[26:27] op_sel_hi:[1,0]
	v_fmac_f32_e32 v30, v52, v52
	v_fmac_f32_e32 v30, v50, v50
	v_fmac_f32_e32 v30, v51, v51
	v_pk_mul_f32 v[32:33], v[114:115], s[26:27] op_sel_hi:[1,0]
	v_add_f32_e32 v118, v54, v30
	v_mul_f32_e32 v54, v33, v33
	v_pk_mul_f32 v[30:31], v[116:117], s[26:27] op_sel_hi:[1,0]
	v_fmac_f32_e32 v54, v32, v32
	v_fmac_f32_e32 v54, v30, v30
	v_fmac_f32_e32 v54, v31, v31
	v_add_f32_e32 v119, v55, v54
	v_mov_b32_e32 v54, v92
	v_mov_b32_e32 v116, v118
	s_nop 0
	v_permlane16_swap_b32_e32 v92, v54
	v_permlane16_swap_b32_e32 v118, v116
	v_add_f32_e32 v54, v92, v54
	v_mov_b32_e32 v92, v93
	v_mov_b32_e32 v114, v122
	v_add_f32_e32 v116, v118, v116
	v_mov_b32_e32 v118, v119
	v_permlane16_swap_b32_e32 v93, v92
	v_permlane16_swap_b32_e32 v122, v114
	v_permlane16_swap_b32_e32 v119, v118
	v_add_f32_e32 v92, v93, v92
	v_add_f32_e32 v114, v122, v114
	v_add_f32_e32 v118, v119, v118
	v_mov_b32_e32 v55, v54
	v_mov_b32_e32 v93, v92
	v_mov_b32_e32 v115, v114
	v_mov_b32_e32 v117, v116
	v_mov_b32_e32 v119, v118
	v_permlane32_swap_b32_e32 v54, v55
	v_permlane32_swap_b32_e32 v92, v93
	v_permlane32_swap_b32_e32 v114, v115
	v_permlane32_swap_b32_e32 v116, v117
	v_permlane32_swap_b32_e32 v118, v119
	v_cmp_gt_u32_e32 vcc, 16, v223
	s_and_saveexec_b64 s[0:1], vcc
	s_cbranch_execz .LBB0_730
	v_add_f32_e32 v92, v92, v93
	v_add_f32_e32 v54, v54, v55
	v_lshl_add_u32 v55, v223, 2, s27
	v_add_f32_e32 v118, v118, v119
	v_add_f32_e32 v116, v116, v117
	v_add_f32_e32 v114, v114, v115
	ds_write2_b32 v55, v54, v92 offset1:16
	ds_write2_b32 v55, v114, v116 offset0:32 offset1:48
	ds_write_b32 v55, v118 offset:256
